# v039 + MLA next-segment LDS addresses computed behind the last MFMA (M end) instead of in the softmax segment tail
# baseline (speedup 1.0000x reference)
; #define SBAR() __builtin_amdgcn_sched_barrier(0)
; __device__ __forceinline__ int kg(int row) { return (row >> 1) & 7; }
; __device__ __forceinline__ int v_rd_base(int lane) { return ((lane & 3) << 3) | (((lane >> 2) & 3) << 6) | (((lane >> 4) & 1) << 5) | (((lane >> 5) & 1) << 8); }
; #define BAR_ALL() asm volatile("s_waitcnt lgkmcnt(0)\n\ts_barrier" ::: "memory")
; #define LWN1(a) do { if constexpr (NW == 0) LW1(0, a); else if constexpr (NW == 1) LW1(1, a); else if constexpr (NW == 2) LW1(2, a); else if constexpr (NW == 3) LW1(3, a); else if constexpr (NW == 4) LW1(4, a); else if constexpr (NW == 5) LW1(5, a); else LW1(6, a); } while (0)
; #define DMA_K(tile, b) DMA_KP(Kh, tile, b)
; #define DMA_V(tile, b) DMA_VP(Vh, tile, b)
; template <int DQK, bool HASQK, bool HASPV, int J> ...
;     ...
;     if constexpr (J < NS) {
;         constexpr int rd1 = (J + 1 < NS) ? ((J + 1 < NQS) ? 1 : 2) : 0, rd2 = (J + 2 < NS) ? ((J + 2 < NQS) ? 1 : 2) : 0, rd3 = (J + 3 < NS) ? ((J + 3 < NQS) ? 1 : 2) : 0, NW = rd1 + rd2 + rd3;
;     ...
;         if constexpr (J < NQS) { constexpr int d0 = J >> 1, h = J & 1;
;             LWN1(kf[d0][h]); SBAR();
;             if constexpr (h == 0) p0 = __builtin_amdgcn_mfma_f32_32x32x16_bf16(kf[d0][0], qr[d0], (d0 == 0) ? negm : p0, 0, 0, 0);
;             else p1 = __builtin_amdgcn_mfma_f32_32x32x16_bf16(kf[d0][1], qr[d0], (d0 == 0) ? negm : p1, 0, 0, 0);
;         } else { constexpr int q = J - NQS, g = q >> 2, d = q & 3;
;             LWN2(vf[g][2 * d], vf[g][2 * d + 1]); SBAR();
;             o[d] = __builtin_amdgcn_mfma_f32_32x32x16_bf16(pa[g], (bf16x8){vf[g][2 * d][0], vf[g][2 * d][1], vf[g][2 * d][2], vf[g][2 * d][3], vf[g][2 * d + 1][0], vf[g][2 * d + 1][1], vf[g][2 * d + 1][2], vf[g][2 * d + 1][3]}, o[d], 0, 0, 0);
;         }
;     ...
;     const int vb0 = (int)(uintptr_t)V_lds + v_rd_base(lane);
;     int ka[4];
; #pragma unroll
;     for (int b = 0; b < 4; ++b) ka[b] = (int)(uintptr_t)lds + r32 * RB + ((b * 32 + hi * 16) ^ (kg(r32) << 4));
;     f32x16 p0, p1; bf16x8 pa0, pa1, pa2, pa3;
;     asm volatile("s_waitcnt vmcnt(0)" ::: "memory"); BAR_ALL();
;     if (ATT_SKEW && g == 1) BAR_ALL();
;     ...
;     int ci = 0;
;     if (DMA_M) { DMA_K(2, 2); DMA_V(1, 1); }
;     SEG_M(true, false, 0, 0); BAR_ALL();
.LBB0_602:
	v_lshlrev_b32_e32 v26, 3, v200
	v_and_b32_e32 v23, 0xc0, v23
	s_cmp_lg_u32 0, -1
	v_and_or_b32 v23, v26, 24, v23
	v_and_b32_e32 v24, 32, v24
	v_and_b32_e32 v27, 0x100, v26
	s_cselect_b32 s10, 0, 0
	v_or3_b32 v23, v23, v24, v27
	v_mov_b32_e32 v24, s10
	s_movk_i32 s11, 0x180
	v_lshlrev_b32_e32 v177, 4, v25
	v_mad_u32_u24 v24, v22, s11, v24
	v_and_b32_e32 v25, 0x70, v26
	v_add_u32_e32 v26, 32, v177
	v_xad_u32 v187, v26, v25, v24
	v_add_u32_e32 v26, 64, v177
	v_xad_u32 v205, v26, v25, v24
	v_add_u32_e32 v26, 0x60, v177
	v_xad_u32 v185, v177, v25, v24
	v_xad_u32 v206, v26, v25, v24
	ds_read_b128 v[24:27], v185 offset:0
	ds_read_b128 v[28:31], v185 offset:0x3000
	ds_read_b128 v[32:35], v187 offset:0
	ds_read_b128 v[36:39], v187 offset:0x3000
	s_add_i32 s10, s10, 0x12000
	s_mov_b32 s26, 0
	v_add_u32_e32 v202, s10, v23
	v_mov_b64_e32 v[94:95], v[14:15]
	v_mov_b64_e32 v[92:93], v[12:13]
	v_mov_b64_e32 v[90:91], v[10:11]
	v_mov_b64_e32 v[88:89], v[8:9]
	v_mov_b64_e32 v[86:87], v[6:7]
	v_mov_b64_e32 v[84:85], v[4:5]
	v_mov_b64_e32 v[82:83], v[2:3]
	v_mov_b64_e32 v[80:81], v[0:1]
	s_waitcnt lgkmcnt(3)
	s_waitcnt vmcnt(0)
	s_nop 0
	v_mfma_f32_32x32x16_bf16 v[96:111], v[24:27], v[112:115], v[80:95]
	ds_read_b128 v[24:27], v205 offset:0
	s_waitcnt lgkmcnt(3)
	s_nop 0
	v_mfma_f32_32x32x16_bf16 v[80:95], v[28:31], v[112:115], v[80:95]
	ds_read_b128 v[28:31], v205 offset:0x3000
	s_waitcnt lgkmcnt(3)
	s_nop 0
	v_mfma_f32_32x32x16_bf16 v[96:111], v[32:35], v[116:119], v[96:111]
	ds_read_b128 v[32:35], v206 offset:0
	s_waitcnt lgkmcnt(3)
	s_nop 0
	v_mfma_f32_32x32x16_bf16 v[80:95], v[36:39], v[116:119], v[80:95]
	ds_read_b128 v[36:39], v206 offset:0x3000
	s_waitcnt lgkmcnt(3)
	s_nop 0
	v_mfma_f32_32x32x16_bf16 v[96:111], v[24:27], v[120:123], v[96:111]
	ds_read_b128 v[24:27], v185 offset:0x80
	s_waitcnt lgkmcnt(3)
	s_nop 0
	v_mfma_f32_32x32x16_bf16 v[80:95], v[28:31], v[120:123], v[80:95]
	ds_read_b128 v[28:31], v185 offset:0x3080
	s_waitcnt lgkmcnt(3)
	s_nop 0
	v_mfma_f32_32x32x16_bf16 v[96:111], v[32:35], v[124:127], v[96:111]
	ds_read_b128 v[32:35], v187 offset:0x80
	s_waitcnt lgkmcnt(3)
	s_nop 0
	v_mfma_f32_32x32x16_bf16 v[80:95], v[36:39], v[124:127], v[80:95]
	ds_read_b128 v[36:39], v187 offset:0x3080
	s_waitcnt lgkmcnt(3)
	s_nop 0
	v_mfma_f32_32x32x16_bf16 v[96:111], v[24:27], v[128:131], v[96:111]
	ds_read_b128 v[24:27], v205 offset:0x80
	s_waitcnt lgkmcnt(3)
	s_nop 0
	v_mfma_f32_32x32x16_bf16 v[80:95], v[28:31], v[128:131], v[80:95]
	ds_read_b128 v[28:31], v205 offset:0x3080
	s_waitcnt lgkmcnt(3)
	s_nop 0
	v_mfma_f32_32x32x16_bf16 v[96:111], v[32:35], v[132:135], v[96:111]
	ds_read_b128 v[32:35], v206 offset:0x80
	s_waitcnt lgkmcnt(3)
	s_nop 0
	v_mfma_f32_32x32x16_bf16 v[80:95], v[36:39], v[132:135], v[80:95]
	ds_read_b128 v[36:39], v206 offset:0x3080
	s_waitcnt lgkmcnt(3)
	s_nop 0
	v_mfma_f32_32x32x16_bf16 v[96:111], v[24:27], v[136:139], v[96:111]
	ds_read_b128 v[24:27], v185 offset:0x100
	s_waitcnt lgkmcnt(3)
	s_nop 0
	v_mfma_f32_32x32x16_bf16 v[80:95], v[28:31], v[136:139], v[80:95]
	ds_read_b128 v[28:31], v185 offset:0x3100
	s_waitcnt lgkmcnt(3)
	s_nop 0
	v_mfma_f32_32x32x16_bf16 v[96:111], v[32:35], v[140:143], v[96:111]
	ds_read_b128 v[32:35], v187 offset:0x100
	s_waitcnt lgkmcnt(3)
	s_nop 0
	v_mfma_f32_32x32x16_bf16 v[80:95], v[36:39], v[140:143], v[80:95]
	ds_read_b128 v[36:39], v187 offset:0x3100
	s_waitcnt lgkmcnt(3)
	s_nop 0
	v_mfma_f32_32x32x16_bf16 v[96:111], v[24:27], v[144:147], v[96:111]
	ds_read_b128 v[24:27], v205 offset:0x100
	s_waitcnt lgkmcnt(3)
	s_nop 0
	v_mfma_f32_32x32x16_bf16 v[80:95], v[28:31], v[144:147], v[80:95]
	ds_read_b128 v[28:31], v205 offset:0x3100
	s_waitcnt lgkmcnt(3)
	s_nop 0
	v_mfma_f32_32x32x16_bf16 v[96:111], v[32:35], v[148:151], v[96:111]
	ds_read_b128 v[32:35], v206 offset:0x100
	s_waitcnt lgkmcnt(3)
	s_nop 0
	v_mfma_f32_32x32x16_bf16 v[80:95], v[36:39], v[148:151], v[80:95]
	ds_read_b128 v[36:39], v206 offset:0x3100
	s_waitcnt lgkmcnt(3)
	s_nop 0
	v_mfma_f32_32x32x16_bf16 v[96:111], v[24:27], v[152:155], v[96:111]
	s_waitcnt lgkmcnt(2)
	s_nop 0
	v_mfma_f32_32x32x16_bf16 v[80:95], v[28:31], v[152:155], v[80:95]
	s_waitcnt lgkmcnt(1)
	s_nop 0
	v_mfma_f32_32x32x16_bf16 v[96:111], v[32:35], v[156:159], v[96:111]
	s_waitcnt lgkmcnt(0)
	s_nop 0
	v_mfma_f32_32x32x16_bf16 v[80:95], v[36:39], v[156:159], v[80:95]
	s_mul_i32 s53, s46, 0x180
	s_add_u32 s52, s52, s53
	s_addc_u32 s47, s47, 0
	s_add_u32 s52, s79, s52
	s_addc_u32 s53, s80, s47
	s_lshl_b32 s46, s46, 8
	s_add_u32 s44, s44, s46
	v_lshlrev_b32_e32 v20, 2, v20
	v_lshlrev_b32_e32 v17, 2, v17
	s_addc_u32 s45, s45, 0
	v_and_b32_e32 v20, 0xffffe000, v20
	v_lshlrev_b32_e32 v18, 10, v18
	v_and_b32_e32 v17, 0xffffe000, v17
	v_or3_b32 v20, v20, v18, v21
	s_add_u32 s44, s81, s44
	v_or3_b32 v17, v17, v18, v19
	s_waitcnt lgkmcnt(0)
	s_barrier
	v_add_u32_e32 v20, v20, v16
	v_mov_b32_e32 v21, v179
	s_addc_u32 s45, s82, s45
	v_add_u32_e32 v16, v17, v16
	v_mov_b32_e32 v17, v179
	v_mov_b32_e32 v64, v179
	v_mov_b32_e32 v65, v179
	v_lshl_add_u32 v201, v22, 2, s67
	v_mov_b32_e32 v181, v179
	v_mov_b32_e32 v183, v179
	v_lshl_add_u64 v[194:195], s[44:45], 0, v[20:21]
	v_lshl_add_u64 v[196:197], s[44:45], 0, v[16:17]
	v_mov_b32_e32 v66, v179
	v_mov_b32_e32 v67, v179
	v_mov_b32_e32 v68, v179
	v_mov_b32_e32 v69, v179
	v_mov_b32_e32 v70, v179
	v_mov_b32_e32 v71, v179
	v_mov_b32_e32 v72, v179
	v_mov_b32_e32 v73, v179
	v_mov_b32_e32 v74, v179
	v_mov_b32_e32 v75, v179
	v_mov_b32_e32 v76, v179
	v_mov_b32_e32 v77, v179
	v_mov_b32_e32 v78, v179
	v_mov_b32_e32 v79, v179
	v_mov_b64_e32 v[48:49], v[64:65]
	v_mov_b64_e32 v[32:33], v[64:65]
	v_mov_b64_e32 v[16:17], v[64:65]
	v_cmp_gt_u32_e64 s[10:11], 32, v200
	v_lshl_add_u64 v[188:189], s[52:53], 0, v[178:179]
	v_lshl_add_u64 v[190:191], s[52:53], 0, v[180:181]
	v_lshl_add_u64 v[192:193], s[52:53], 0, v[182:183]
	v_mov_b32_e32 v204, 0
	s_mov_b64 s[44:45], 0
	v_mov_b64_e32 v[50:51], v[66:67]
	v_mov_b64_e32 v[52:53], v[68:69]
	v_mov_b64_e32 v[54:55], v[70:71]
	v_mov_b64_e32 v[56:57], v[72:73]
	v_mov_b64_e32 v[58:59], v[74:75]
	v_mov_b64_e32 v[60:61], v[76:77]
	v_mov_b64_e32 v[62:63], v[78:79]
	v_mov_b64_e32 v[34:35], v[66:67]
	v_mov_b64_e32 v[36:37], v[68:69]
	v_mov_b64_e32 v[38:39], v[70:71]
	v_mov_b64_e32 v[40:41], v[72:73]
	v_mov_b64_e32 v[42:43], v[74:75]
	v_mov_b64_e32 v[44:45], v[76:77]
	v_mov_b64_e32 v[46:47], v[78:79]
	v_mov_b64_e32 v[18:19], v[66:67]
	v_mov_b64_e32 v[20:21], v[68:69]
	v_mov_b64_e32 v[22:23], v[70:71]
	v_mov_b64_e32 v[24:25], v[72:73]
	v_mov_b64_e32 v[26:27], v[74:75]
	v_mov_b64_e32 v[28:29], v[76:77]
	v_mov_b64_e32 v[30:31], v[78:79]
	v_mov_b32_e32 v203, 0
	s_add_i32 s46, s26, 1
	s_cmp_lg_u32 s26, 2
	s_cselect_b32 s46, s46, 0
	s_mul_i32 s47, s46, 0x6000
	s_lshl_b32 s46, s26, 14
	v_add_u32_e32 v227, s46, v202
	v_add_u32_e32 v207, s47, v185
	v_add_u32_e32 v224, s47, v187
	v_add_u32_e32 v225, s47, v205
	v_add_u32_e32 v226, s47, v206
	s_branch .LBB0_606

; #define PK4(P, BASE, OUT) do { u32x4 w = {cvtpk(P[BASE + 0], P[BASE + 1]), cvtpk(P[BASE + 2], P[BASE + 3]), cvtpk(P[BASE + 4], P[BASE + 5]), cvtpk(P[BASE + 6], P[BASE + 7])}; \
;     OUT = *reinterpret_cast<bf16x8*>(&w); } while (0)
; __device__ __forceinline__ void smax_tile(f32x16& p0, f32x16& p1, float& mhat, float& l_reg, f32x16 (&o)[4], float* al_l, const bool first, int r32, int hi,
;                                           bf16x8& pa0, bf16x8& pa1, bf16x8& pa2, bf16x8& pa3) {
;     ...
; #pragma unroll
;     for (int r = 0; r < 16; ++r) p0[r] = __builtin_amdgcn_exp2f(p0[r]);
; #pragma unroll
;     for (int r = 0; r < 16; ++r) p1[r] = __builtin_amdgcn_exp2f(p1[r]);
;     float ps = p0[0];
; #pragma unroll
;     for (int r = 1; r < 16; ++r) ps += p0[r];
; #pragma unroll
;     for (int r = 0; r < 16; ++r) ps += p1[r];
;     { auto rr = __builtin_amdgcn_permlane32_swap(__float_as_uint(ps), __float_as_uint(ps), false, false); ps = __uint_as_float(rr[0]) + __uint_as_float(rr[1]); }
;     l_reg += ps;
;     ...
;     PK4(p0, 0, pa0); PK4(p0, 8, pa1); PK4(p1, 0, pa2); PK4(p1, 8, pa3);
.LBB0_605:
	v_exp_f32_e32 v96, v96
	v_exp_f32_e32 v97, v97
	v_exp_f32_e32 v98, v98
	v_exp_f32_e32 v99, v99
	v_exp_f32_e32 v100, v100
	v_exp_f32_e32 v101, v101
	v_add_f32_e32 v160, v96, v97
	v_exp_f32_e32 v102, v102
	v_add_f32_e32 v160, v98, v160
	v_exp_f32_e32 v103, v103
	v_add_f32_e32 v160, v99, v160
	v_exp_f32_e32 v104, v104
	v_add_f32_e32 v160, v100, v160
	v_exp_f32_e32 v105, v105
	v_add_f32_e32 v160, v101, v160
	v_exp_f32_e32 v106, v106
	v_add_f32_e32 v160, v102, v160
	v_exp_f32_e32 v107, v107
	v_add_f32_e32 v160, v103, v160
	v_exp_f32_e32 v108, v108
	v_add_f32_e32 v160, v104, v160
	v_exp_f32_e32 v109, v109
	v_add_f32_e32 v160, v105, v160
	v_exp_f32_e32 v110, v110
	v_add_f32_e32 v160, v106, v160
	v_exp_f32_e32 v111, v111
	v_add_f32_e32 v160, v107, v160
	v_exp_f32_e32 v80, v80
	v_add_f32_e32 v160, v108, v160
	v_exp_f32_e32 v81, v81
	v_add_f32_e32 v160, v109, v160
	v_exp_f32_e32 v82, v82
	v_add_f32_e32 v160, v110, v160
	v_exp_f32_e32 v83, v83
	v_add_f32_e32 v160, v111, v160
	v_exp_f32_e32 v84, v84
	v_add_f32_e32 v160, v80, v160
	v_exp_f32_e32 v85, v85
	v_add_f32_e32 v160, v81, v160
	v_exp_f32_e32 v86, v86
	v_add_f32_e32 v160, v82, v160
	v_exp_f32_e32 v87, v87
	v_add_f32_e32 v160, v83, v160
	v_exp_f32_e32 v88, v88
	v_add_f32_e32 v160, v84, v160
	v_exp_f32_e32 v89, v89
	v_add_f32_e32 v160, v85, v160
	v_exp_f32_e32 v90, v90
	v_add_f32_e32 v160, v86, v160
	v_exp_f32_e32 v91, v91
	v_add_f32_e32 v160, v87, v160
	v_exp_f32_e32 v92, v92
	v_add_f32_e32 v160, v88, v160
	v_exp_f32_e32 v93, v93
	v_add_f32_e32 v160, v89, v160
	v_exp_f32_e32 v94, v94
	v_add_f32_e32 v160, v90, v160
	v_exp_f32_e32 v95, v95
	v_add_f32_e32 v160, v91, v160
	v_add_f32_e32 v160, v92, v160
	v_add_f32_e32 v160, v93, v160
	v_add_f32_e32 v160, v94, v160
	v_add_f32_e32 v160, v95, v160
	v_mov_b32_e32 v161, v160
	v_cvt_pk_bf16_f32 v172, v96, v97
	v_cvt_pk_bf16_f32 v173, v98, v99
	v_permlane32_swap_b32_e32 v160, v161
	v_add_f32_e32 v160, v160, v161
	v_add_f32_e32 v204, v204, v160
	v_cvt_pk_bf16_f32 v174, v100, v101
	v_cvt_pk_bf16_f32 v175, v102, v103
	v_cvt_pk_bf16_f32 v168, v104, v105
	v_cvt_pk_bf16_f32 v169, v106, v107
	v_cvt_pk_bf16_f32 v170, v108, v109
	v_cvt_pk_bf16_f32 v171, v110, v111
	v_cvt_pk_bf16_f32 v164, v80, v81
	v_cvt_pk_bf16_f32 v165, v82, v83
	v_cvt_pk_bf16_f32 v166, v84, v85
	v_cvt_pk_bf16_f32 v167, v86, v87
	v_cvt_pk_bf16_f32 v160, v88, v89
	v_cvt_pk_bf16_f32 v161, v90, v91
	v_cvt_pk_bf16_f32 v162, v92, v93
	v_cvt_pk_bf16_f32 v163, v94, v95
	s_waitcnt lgkmcnt(0)
	ds_read_b64_tr_b16 v[208:209], v227 offset:0
	ds_read_b64_tr_b16 v[210:211], v227 offset:2048
	ds_read_b64_tr_b16 v[212:213], v227 offset:512
	ds_read_b64_tr_b16 v[214:215], v227 offset:2560
	ds_read_b64_tr_b16 v[216:217], v227 offset:1024
	ds_read_b64_tr_b16 v[218:219], v227 offset:3072
	ds_read_b64_tr_b16 v[220:221], v227 offset:1536
	ds_read_b64_tr_b16 v[222:223], v227 offset:3584
	s_barrier
; #define SBAR() __builtin_amdgcn_sched_barrier(0)
; #define LWN1(a) do { if constexpr (NW == 0) LW1(0, a); else if constexpr (NW == 1) LW1(1, a); else if constexpr (NW == 2) LW1(2, a); else if constexpr (NW == 3) LW1(3, a); else if constexpr (NW == 4) LW1(4, a); else if constexpr (NW == 5) LW1(5, a); else LW1(6, a); } while (0)
; #define LWN2(a, b) do { if constexpr (NW == 0) LW2(0, a, b); else if constexpr (NW == 1) LW2(1, a, b); else if constexpr (NW == 2) LW2(2, a, b); else if constexpr (NW == 3) LW2(3, a, b); else if constexpr (NW == 4) LW2(4, a, b); else if constexpr (NW == 5) LW2(5, a, b); else LW2(6, a, b); } while (0)
; template <int DQK, bool HASQK, bool HASPV, int J> ...
;     constexpr int NQS = HASQK ? 2 * (DQK / 16) : 0, NS = NQS + (HASPV ? 16 : 0);
;     if constexpr (J < NS) {
;         constexpr int rd1 = (J + 1 < NS) ? ((J + 1 < NQS) ? 1 : 2) : 0, rd2 = (J + 2 < NS) ? ((J + 2 < NQS) ? 1 : 2) : 0, rd3 = (J + 3 < NS) ? ((J + 3 < NQS) ? 1 : 2) : 0, NW = rd1 + rd2 + rd3;
;     ...
;         if constexpr (J < NQS) { constexpr int d0 = J >> 1, h = J & 1;
;             LWN1(kf[d0][h]); SBAR();
;             if constexpr (h == 0) p0 = __builtin_amdgcn_mfma_f32_32x32x16_bf16(kf[d0][0], qr[d0], (d0 == 0) ? negm : p0, 0, 0, 0);
;             else p1 = __builtin_amdgcn_mfma_f32_32x32x16_bf16(kf[d0][1], qr[d0], (d0 == 0) ? negm : p1, 0, 0, 0);
;         } else { constexpr int q = J - NQS, g = q >> 2, d = q & 3;
;             LWN2(vf[g][2 * d], vf[g][2 * d + 1]); SBAR();
;             o[d] = __builtin_amdgcn_mfma_f32_32x32x16_bf16(pa[g], (bf16x8){vf[g][2 * d][0], vf[g][2 * d][1], vf[g][2 * d][2], vf[g][2 * d][3], vf[g][2 * d + 1][0], vf[g][2 * d + 1][1], vf[g][2 * d + 1][2], vf[g][2 * d + 1][3]}, o[d], 0, 0, 0);
;         }
;     ...
;         SBAR();
;         slot_read<DQK, HASQK, HASPV, J + 4>(kf, vf, ka_, vb_);
;         SBAR();
;         slot_run<DQK, HASQK, HASPV, J + 1>(kf, vf, ka_, vb_, qr, p0, p1, negm, o, pa);
	s_waitcnt lgkmcnt(6)
	v_mfma_f32_32x32x16_bf16 v[64:79], v[172:175], v[208:211], v[64:79]
	ds_read_b64_tr_b16 v[208:209], v227 offset:4096
	ds_read_b64_tr_b16 v[210:211], v227 offset:6144
	s_waitcnt lgkmcnt(6)
	v_mfma_f32_32x32x16_bf16 v[48:63], v[172:175], v[212:215], v[48:63]
	ds_read_b64_tr_b16 v[212:213], v227 offset:4608
	ds_read_b64_tr_b16 v[214:215], v227 offset:6656
	s_waitcnt lgkmcnt(6)
	v_mfma_f32_32x32x16_bf16 v[32:47], v[172:175], v[216:219], v[32:47]
	ds_read_b64_tr_b16 v[216:217], v227 offset:5120
	ds_read_b64_tr_b16 v[218:219], v227 offset:7168
	s_waitcnt lgkmcnt(6)
	v_mfma_f32_32x32x16_bf16 v[16:31], v[172:175], v[220:223], v[16:31]
	ds_read_b64_tr_b16 v[220:221], v227 offset:5632
	ds_read_b64_tr_b16 v[222:223], v227 offset:7680
	s_waitcnt lgkmcnt(6)
	v_mfma_f32_32x32x16_bf16 v[64:79], v[168:171], v[208:211], v[64:79]
	ds_read_b64_tr_b16 v[208:209], v227 offset:8192
	ds_read_b64_tr_b16 v[210:211], v227 offset:10240
	s_waitcnt lgkmcnt(6)
	v_mfma_f32_32x32x16_bf16 v[48:63], v[168:171], v[212:215], v[48:63]
	ds_read_b64_tr_b16 v[212:213], v227 offset:8704
	ds_read_b64_tr_b16 v[214:215], v227 offset:10752
	s_waitcnt lgkmcnt(6)
	v_mfma_f32_32x32x16_bf16 v[32:47], v[168:171], v[216:219], v[32:47]
	ds_read_b64_tr_b16 v[216:217], v227 offset:9216
	ds_read_b64_tr_b16 v[218:219], v227 offset:11264
	s_waitcnt lgkmcnt(6)
	v_mfma_f32_32x32x16_bf16 v[16:31], v[168:171], v[220:223], v[16:31]
	ds_read_b64_tr_b16 v[220:221], v227 offset:9728
	ds_read_b64_tr_b16 v[222:223], v227 offset:11776
	s_waitcnt lgkmcnt(6)
	v_mfma_f32_32x32x16_bf16 v[64:79], v[164:167], v[208:211], v[64:79]
	ds_read_b64_tr_b16 v[208:209], v227 offset:12288
	ds_read_b64_tr_b16 v[210:211], v227 offset:14336
	s_waitcnt lgkmcnt(6)
	v_mfma_f32_32x32x16_bf16 v[48:63], v[164:167], v[212:215], v[48:63]
	ds_read_b64_tr_b16 v[212:213], v227 offset:12800
	ds_read_b64_tr_b16 v[214:215], v227 offset:14848
	s_waitcnt lgkmcnt(6)
	v_mfma_f32_32x32x16_bf16 v[32:47], v[164:167], v[216:219], v[32:47]
	ds_read_b64_tr_b16 v[216:217], v227 offset:13312
	ds_read_b64_tr_b16 v[218:219], v227 offset:15360
	s_waitcnt lgkmcnt(6)
	v_mfma_f32_32x32x16_bf16 v[16:31], v[164:167], v[220:223], v[16:31]
	ds_read_b64_tr_b16 v[220:221], v227 offset:13824
	ds_read_b64_tr_b16 v[222:223], v227 offset:15872
	v_xor_b32_e32 v80, 0x80000000, v203
	v_mov_b32_e32 v81, v80
	v_mov_b32_e32 v82, v80
	v_mov_b32_e32 v83, v80
	v_mov_b32_e32 v84, v80
	v_mov_b32_e32 v85, v80
	v_mov_b32_e32 v86, v80
	v_mov_b32_e32 v87, v80
	v_mov_b32_e32 v88, v80
	v_mov_b32_e32 v89, v80
	v_mov_b32_e32 v90, v80
	v_mov_b32_e32 v91, v80
	v_mov_b32_e32 v92, v80
	v_mov_b32_e32 v93, v80
	v_mov_b32_e32 v94, v80
	v_mov_b32_e32 v95, v80
	s_waitcnt lgkmcnt(6)
	v_mfma_f32_32x32x16_bf16 v[64:79], v[160:163], v[208:211], v[64:79]
	ds_read_b128 v[208:211], v207 offset:0
	s_waitcnt lgkmcnt(5)
	v_mfma_f32_32x32x16_bf16 v[48:63], v[160:163], v[212:215], v[48:63]
	ds_read_b128 v[212:215], v207 offset:12288
	s_waitcnt lgkmcnt(4)
	v_mfma_f32_32x32x16_bf16 v[32:47], v[160:163], v[216:219], v[32:47]
	ds_read_b128 v[216:219], v224 offset:0
	s_waitcnt lgkmcnt(3)
	v_mfma_f32_32x32x16_bf16 v[16:31], v[160:163], v[220:223], v[16:31]
	ds_read_b128 v[220:223], v224 offset:12288
	s_waitcnt lgkmcnt(3)
	v_mfma_f32_32x32x16_bf16 v[96:111], v[208:211], v[112:115], v[80:95]
	ds_read_b128 v[208:211], v225 offset:0
	s_waitcnt lgkmcnt(3)
	v_mfma_f32_32x32x16_bf16 v[80:95], v[212:215], v[112:115], v[80:95]
	ds_read_b128 v[212:215], v225 offset:12288
	s_waitcnt lgkmcnt(3)
	v_mfma_f32_32x32x16_bf16 v[96:111], v[216:219], v[116:119], v[96:111]
	ds_read_b128 v[216:219], v226 offset:0
	s_waitcnt lgkmcnt(3)
	v_mfma_f32_32x32x16_bf16 v[80:95], v[220:223], v[116:119], v[80:95]
	ds_read_b128 v[220:223], v226 offset:12288
	s_waitcnt lgkmcnt(3)
	v_mfma_f32_32x32x16_bf16 v[96:111], v[208:211], v[120:123], v[96:111]
	ds_read_b128 v[208:211], v207 offset:128
	s_waitcnt lgkmcnt(3)
	v_mfma_f32_32x32x16_bf16 v[80:95], v[212:215], v[120:123], v[80:95]
	ds_read_b128 v[212:215], v207 offset:12416
	s_waitcnt lgkmcnt(3)
	v_mfma_f32_32x32x16_bf16 v[96:111], v[216:219], v[124:127], v[96:111]
	ds_read_b128 v[216:219], v224 offset:128
	s_waitcnt lgkmcnt(3)
	v_mfma_f32_32x32x16_bf16 v[80:95], v[220:223], v[124:127], v[80:95]
	ds_read_b128 v[220:223], v224 offset:12416
	s_waitcnt lgkmcnt(3)
	v_mfma_f32_32x32x16_bf16 v[96:111], v[208:211], v[128:131], v[96:111]
	ds_read_b128 v[208:211], v225 offset:128
	s_waitcnt lgkmcnt(3)
	v_mfma_f32_32x32x16_bf16 v[80:95], v[212:215], v[128:131], v[80:95]
	ds_read_b128 v[212:215], v225 offset:12416
	s_waitcnt lgkmcnt(3)
	v_mfma_f32_32x32x16_bf16 v[96:111], v[216:219], v[132:135], v[96:111]
	ds_read_b128 v[216:219], v226 offset:128
	s_waitcnt lgkmcnt(3)
	v_mfma_f32_32x32x16_bf16 v[80:95], v[220:223], v[132:135], v[80:95]
	ds_read_b128 v[220:223], v226 offset:12416
	s_waitcnt lgkmcnt(3)
	v_mfma_f32_32x32x16_bf16 v[96:111], v[208:211], v[136:139], v[96:111]
	ds_read_b128 v[208:211], v207 offset:256
	s_waitcnt lgkmcnt(3)
	v_mfma_f32_32x32x16_bf16 v[80:95], v[212:215], v[136:139], v[80:95]
	ds_read_b128 v[212:215], v207 offset:12544
	s_waitcnt lgkmcnt(3)
	v_mfma_f32_32x32x16_bf16 v[96:111], v[216:219], v[140:143], v[96:111]
	ds_read_b128 v[216:219], v224 offset:256
	s_waitcnt lgkmcnt(3)
	v_mfma_f32_32x32x16_bf16 v[80:95], v[220:223], v[140:143], v[80:95]
	ds_read_b128 v[220:223], v224 offset:12544
	s_waitcnt lgkmcnt(3)
	v_mfma_f32_32x32x16_bf16 v[96:111], v[208:211], v[144:147], v[96:111]
	ds_read_b128 v[208:211], v225 offset:256
	s_waitcnt lgkmcnt(3)
	v_mfma_f32_32x32x16_bf16 v[80:95], v[212:215], v[144:147], v[80:95]
	ds_read_b128 v[212:215], v225 offset:12544
	s_waitcnt lgkmcnt(3)
	v_mfma_f32_32x32x16_bf16 v[96:111], v[216:219], v[148:151], v[96:111]
	ds_read_b128 v[216:219], v226 offset:256
	s_waitcnt lgkmcnt(3)
	v_mfma_f32_32x32x16_bf16 v[80:95], v[220:223], v[148:151], v[80:95]
	ds_read_b128 v[220:223], v226 offset:12544
	s_waitcnt lgkmcnt(3)
	v_mfma_f32_32x32x16_bf16 v[96:111], v[208:211], v[152:155], v[96:111]
	s_waitcnt lgkmcnt(2)
	v_mfma_f32_32x32x16_bf16 v[80:95], v[212:215], v[152:155], v[80:95]
	s_waitcnt lgkmcnt(1)
	v_mfma_f32_32x32x16_bf16 v[96:111], v[216:219], v[156:159], v[96:111]
	s_waitcnt lgkmcnt(0)
	v_mfma_f32_32x32x16_bf16 v[80:95], v[220:223], v[156:159], v[80:95]
	s_add_i32 s46, s26, 1
	s_cmp_lg_u32 s26, 2
	s_cselect_b32 s46, s46, 0
	s_mul_i32 s47, s46, 0x6000
	s_lshl_b32 s46, s26, 14
	v_add_u32_e32 v227, s46, v202
	v_add_u32_e32 v207, s47, v185
	v_add_u32_e32 v224, s47, v187
	v_add_u32_e32 v225, s47, v205
	v_add_u32_e32 v226, s47, v206
	s_waitcnt vmcnt(0)
	s_waitcnt lgkmcnt(0)
	s_barrier
	s_add_u32 s44, s44, 0x18000
	s_addc_u32 s45, s45, 0
	v_lshl_add_u64 v[194:195], v[194:195], 0, s[28:29]
	s_cmp_eq_u32 s44, 0xbe8000
	v_lshl_add_u64 v[196:197], v[196:197], 0, s[28:29]
	s_cbranch_scc1 .LBB0_616
